# v3 + grid barrier: non-last workgroups poll the top-level generation word directly, per-XCD generation bump dropped
# speedup vs baseline: 1.0092x; 1.0092x over previous
.LBB0_50:
	s_or_b64 exec, exec, s[8:9]
	v_cvt_f32_u32_e32 v4, v2
	s_waitcnt vmcnt(0)
	v_readfirstlane_b32 s6, v3
	v_sub_u32_e32 v3, 0, v2
	v_rcp_iflag_f32_e32 v4, v4
	v_add_u32_e32 v5, s6, v1
	v_mul_f32_e32 v4, 0x4f7ffffe, v4
	v_cvt_u32_f32_e32 v4, v4
	v_mul_lo_u32 v1, v3, v4
	v_mul_hi_u32 v1, v4, v1
	v_add_u32_e32 v1, v4, v1
	v_mul_hi_u32 v1, v5, v1
	v_mul_lo_u32 v3, v1, v2
	v_sub_u32_e32 v3, v5, v3
	v_add_u32_e32 v4, 1, v1
	v_cmp_ge_u32_e32 vcc, v3, v2
	s_nop 1
	v_cndmask_b32_e32 v1, v1, v4, vcc
	v_sub_u32_e32 v4, v3, v2
	v_cndmask_b32_e32 v3, v3, v4, vcc
	v_add_u32_e32 v4, 1, v1
	v_cmp_ge_u32_e32 vcc, v3, v2
	v_add_u32_e32 v3, 1, v5
	s_nop 0
	v_cndmask_b32_e32 v1, v1, v4, vcc
	v_mul_lo_u32 v4, v2, v1
	v_add_u32_e32 v2, v4, v2
	v_cmp_ne_u32_e32 vcc, v3, v2
	s_and_saveexec_b64 s[6:7], vcc
	s_xor_b64 s[6:7], exec, s[6:7]
	s_cbranch_execz .LBB0_64
	s_waitcnt lgkmcnt(0)
	v_mov_b32_e32 v0, 0x7000
	global_load_dword v0, v0, s[54:55] offset:1280 sc1
	s_add_u32 s28, s54, 0x7500
	s_addc_u32 s29, s55, 0
	s_waitcnt vmcnt(0)
	v_cmp_eq_u32_e32 vcc, v0, v1
	s_and_saveexec_b64 s[8:9], vcc
	s_cbranch_execz .LBB0_63
	s_add_u32 s10, s54, 0x4200
	s_addc_u32 s11, s55, 0
	s_mov_b32 s60, 1
	s_mov_b64 s[30:31], 0
	v_mov_b32_e32 v0, 0
	s_branch .LBB0_54

.LBB0_81:
	s_or_b64 exec, exec, s[6:7]
	s_mov_b64 s[6:7], exec
	v_mbcnt_lo_u32_b32 v0, s6, 0
	v_mbcnt_hi_u32_b32 v0, s7, v0
	v_cmp_eq_u32_e32 vcc, 0, v0
	s_waitcnt vmcnt(0)
	buffer_inv sc1
	s_and_saveexec_b64 s[8:9], vcc
	s_cbranch_execz .LBB0_83
	s_bcnt1_i32_b64 s6, s[6:7]
	v_mov_b32_e32 v0, 0x2000
	v_mov_b32_e32 v1, s6
	s_nop 0
	s_nop 0

.LBB0_368:
	s_or_b64 exec, exec, s[8:9]
	v_cvt_f32_u32_e32 v4, v2
	s_waitcnt vmcnt(0)
	v_readfirstlane_b32 s6, v3
	v_sub_u32_e32 v3, 0, v2
	v_rcp_iflag_f32_e32 v4, v4
	v_add_u32_e32 v5, s6, v1
	v_mul_f32_e32 v4, 0x4f7ffffe, v4
	v_cvt_u32_f32_e32 v4, v4
	v_mul_lo_u32 v1, v3, v4
	v_mul_hi_u32 v1, v4, v1
	v_add_u32_e32 v1, v4, v1
	v_mul_hi_u32 v1, v5, v1
	v_mul_lo_u32 v3, v1, v2
	v_sub_u32_e32 v3, v5, v3
	v_add_u32_e32 v4, 1, v1
	v_cmp_ge_u32_e32 vcc, v3, v2
	s_nop 1
	v_cndmask_b32_e32 v1, v1, v4, vcc
	v_sub_u32_e32 v4, v3, v2
	v_cndmask_b32_e32 v3, v3, v4, vcc
	v_add_u32_e32 v4, 1, v1
	v_cmp_ge_u32_e32 vcc, v3, v2
	v_add_u32_e32 v3, 1, v5
	s_nop 0
	v_cndmask_b32_e32 v1, v1, v4, vcc
	v_mul_lo_u32 v4, v2, v1
	v_add_u32_e32 v2, v4, v2
	v_cmp_ne_u32_e32 vcc, v3, v2
	s_and_saveexec_b64 s[6:7], vcc
	s_xor_b64 s[6:7], exec, s[6:7]
	s_cbranch_execz .LBB0_382
	s_waitcnt lgkmcnt(0)
	v_mov_b32_e32 v0, 0x7000
	global_load_dword v0, v0, s[54:55] offset:1280 sc1
	s_add_u32 s12, s54, 0x7500
	s_addc_u32 s13, s55, 0
	s_waitcnt vmcnt(0)
	v_cmp_eq_u32_e32 vcc, v0, v1
	s_and_saveexec_b64 s[8:9], vcc
	s_cbranch_execz .LBB0_381
	s_add_u32 s10, s54, 0x4200
	s_addc_u32 s11, s55, 0
	s_mov_b32 s30, 1
	s_mov_b64 s[14:15], 0
	v_mov_b32_e32 v0, 0
	s_branch .LBB0_372

.LBB0_545:
	s_or_b64 exec, exec, s[10:11]
	v_cvt_f32_u32_e32 v4, v2
	s_waitcnt vmcnt(0)
	v_readfirstlane_b32 s8, v3
	v_sub_u32_e32 v3, 0, v2
	v_rcp_iflag_f32_e32 v4, v4
	v_add_u32_e32 v5, s8, v1
	v_mul_f32_e32 v4, 0x4f7ffffe, v4
	v_cvt_u32_f32_e32 v4, v4
	v_mul_lo_u32 v1, v3, v4
	v_mul_hi_u32 v1, v4, v1
	v_add_u32_e32 v1, v4, v1
	v_mul_hi_u32 v1, v5, v1
	v_mul_lo_u32 v3, v1, v2
	v_sub_u32_e32 v3, v5, v3
	v_add_u32_e32 v4, 1, v1
	v_cmp_ge_u32_e32 vcc, v3, v2
	s_nop 1
	v_cndmask_b32_e32 v1, v1, v4, vcc
	v_sub_u32_e32 v4, v3, v2
	v_cndmask_b32_e32 v3, v3, v4, vcc
	v_add_u32_e32 v4, 1, v1
	v_cmp_ge_u32_e32 vcc, v3, v2
	v_add_u32_e32 v3, 1, v5
	s_nop 0
	v_cndmask_b32_e32 v1, v1, v4, vcc
	v_mul_lo_u32 v4, v2, v1
	v_add_u32_e32 v2, v4, v2
	v_cmp_ne_u32_e32 vcc, v3, v2
	s_and_saveexec_b64 s[8:9], vcc
	s_xor_b64 s[8:9], exec, s[8:9]
	s_cbranch_execz .LBB0_559
	s_waitcnt lgkmcnt(0)
	v_mov_b32_e32 v0, 0x7000
	global_load_dword v0, v0, s[54:55] offset:1280 sc1
	s_add_u32 s14, s54, 0x7500
	s_addc_u32 s15, s55, 0
	s_waitcnt vmcnt(0)
	v_cmp_eq_u32_e32 vcc, v0, v1
	s_and_saveexec_b64 s[10:11], vcc
	s_cbranch_execz .LBB0_558
	s_add_u32 s12, s54, 0x4200
	s_addc_u32 s13, s55, 0
	s_mov_b32 s34, 1
	s_mov_b64 s[16:17], 0
	v_mov_b32_e32 v0, 0
	s_branch .LBB0_549

.LBB0_576:
	s_or_b64 exec, exec, s[8:9]
	s_mov_b64 s[8:9], exec
	v_mbcnt_lo_u32_b32 v0, s8, 0
	v_mbcnt_hi_u32_b32 v0, s9, v0
	v_cmp_eq_u32_e32 vcc, 0, v0
	s_waitcnt vmcnt(0)
	buffer_inv sc1
	s_and_saveexec_b64 s[10:11], vcc
	s_cbranch_execz .LBB0_578
	s_bcnt1_i32_b64 s8, s[8:9]
	v_mov_b32_e32 v0, 0x2000
	v_mov_b32_e32 v1, s8
	s_nop 0
	s_nop 0

.LBB0_799:
	s_or_b64 exec, exec, s[8:9]
	v_cvt_f32_u32_e32 v4, v2
	s_waitcnt vmcnt(0)
	v_readfirstlane_b32 s6, v3
	v_sub_u32_e32 v3, 0, v2
	v_rcp_iflag_f32_e32 v4, v4
	v_add_u32_e32 v5, s6, v1
	v_mul_f32_e32 v4, 0x4f7ffffe, v4
	v_cvt_u32_f32_e32 v4, v4
	v_mul_lo_u32 v1, v3, v4
	v_mul_hi_u32 v1, v4, v1
	v_add_u32_e32 v1, v4, v1
	v_mul_hi_u32 v1, v5, v1
	v_mul_lo_u32 v3, v1, v2
	v_sub_u32_e32 v3, v5, v3
	v_add_u32_e32 v4, 1, v1
	v_cmp_ge_u32_e32 vcc, v3, v2
	s_nop 1
	v_cndmask_b32_e32 v1, v1, v4, vcc
	v_sub_u32_e32 v4, v3, v2
	v_cndmask_b32_e32 v3, v3, v4, vcc
	v_add_u32_e32 v4, 1, v1
	v_cmp_ge_u32_e32 vcc, v3, v2
	v_add_u32_e32 v3, 1, v5
	s_nop 0
	v_cndmask_b32_e32 v1, v1, v4, vcc
	v_mul_lo_u32 v4, v2, v1
	v_add_u32_e32 v2, v4, v2
	v_cmp_ne_u32_e32 vcc, v3, v2
	s_and_saveexec_b64 s[6:7], vcc
	s_xor_b64 s[6:7], exec, s[6:7]
	s_cbranch_execz .LBB0_813
	s_waitcnt lgkmcnt(0)
	v_mov_b32_e32 v0, 0x7000
	global_load_dword v0, v0, s[54:55] offset:1280 sc1
	s_add_u32 s12, s54, 0x7500
	s_addc_u32 s13, s55, 0
	s_waitcnt vmcnt(0)
	v_cmp_eq_u32_e32 vcc, v0, v1
	s_and_saveexec_b64 s[8:9], vcc
	s_cbranch_execz .LBB0_812
	s_add_u32 s10, s54, 0x4200
	s_addc_u32 s11, s55, 0
	s_mov_b32 s28, 1
	s_mov_b64 s[14:15], 0
	v_mov_b32_e32 v0, 0
	s_branch .LBB0_803

.LBB0_906:
	s_or_b64 exec, exec, s[8:9]
	v_cvt_f32_u32_e32 v4, v2
	s_waitcnt vmcnt(0)
	v_readfirstlane_b32 s6, v3
	v_sub_u32_e32 v3, 0, v2
	v_rcp_iflag_f32_e32 v4, v4
	v_add_u32_e32 v5, s6, v1
	v_mul_f32_e32 v4, 0x4f7ffffe, v4
	v_cvt_u32_f32_e32 v4, v4
	v_mul_lo_u32 v1, v3, v4
	v_mul_hi_u32 v1, v4, v1
	v_add_u32_e32 v1, v4, v1
	v_mul_hi_u32 v1, v5, v1
	v_mul_lo_u32 v3, v1, v2
	v_sub_u32_e32 v3, v5, v3
	v_add_u32_e32 v4, 1, v1
	v_cmp_ge_u32_e32 vcc, v3, v2
	s_nop 1
	v_cndmask_b32_e32 v1, v1, v4, vcc
	v_sub_u32_e32 v4, v3, v2
	v_cndmask_b32_e32 v3, v3, v4, vcc
	v_add_u32_e32 v4, 1, v1
	v_cmp_ge_u32_e32 vcc, v3, v2
	v_add_u32_e32 v3, 1, v5
	s_nop 0
	v_cndmask_b32_e32 v1, v1, v4, vcc
	v_mul_lo_u32 v4, v2, v1
	v_add_u32_e32 v2, v4, v2
	v_cmp_ne_u32_e32 vcc, v3, v2
	s_and_saveexec_b64 s[6:7], vcc
	s_xor_b64 s[6:7], exec, s[6:7]
	s_cbranch_execz .LBB0_920
	s_waitcnt lgkmcnt(0)
	v_mov_b32_e32 v0, 0x7000
	global_load_dword v0, v0, s[54:55] offset:1280 sc1
	s_add_u32 s12, s54, 0x7500
	s_addc_u32 s13, s55, 0
	s_waitcnt vmcnt(0)
	v_cmp_eq_u32_e32 vcc, v0, v1
	s_and_saveexec_b64 s[8:9], vcc
	s_cbranch_execz .LBB0_919
	s_add_u32 s10, s54, 0x4200
	s_addc_u32 s11, s55, 0
	s_mov_b32 s26, 1
	s_mov_b64 s[14:15], 0
	v_mov_b32_e32 v0, 0
	s_branch .LBB0_910

.LBB0_1055:
	s_or_b64 exec, exec, s[8:9]
	v_cvt_f32_u32_e32 v4, v2
	s_waitcnt vmcnt(0)
	v_readfirstlane_b32 s6, v3
	v_sub_u32_e32 v3, 0, v2
	v_rcp_iflag_f32_e32 v4, v4
	v_add_u32_e32 v5, s6, v1
	v_mul_f32_e32 v4, 0x4f7ffffe, v4
	v_cvt_u32_f32_e32 v4, v4
	v_mul_lo_u32 v1, v3, v4
	v_mul_hi_u32 v1, v4, v1
	v_add_u32_e32 v1, v4, v1
	v_mul_hi_u32 v1, v5, v1
	v_mul_lo_u32 v3, v1, v2
	v_sub_u32_e32 v3, v5, v3
	v_add_u32_e32 v4, 1, v1
	v_cmp_ge_u32_e32 vcc, v3, v2
	s_nop 1
	v_cndmask_b32_e32 v1, v1, v4, vcc
	v_sub_u32_e32 v4, v3, v2
	v_cndmask_b32_e32 v3, v3, v4, vcc
	v_add_u32_e32 v4, 1, v1
	v_cmp_ge_u32_e32 vcc, v3, v2
	v_add_u32_e32 v3, 1, v5
	s_nop 0
	v_cndmask_b32_e32 v1, v1, v4, vcc
	v_mul_lo_u32 v4, v2, v1
	v_add_u32_e32 v2, v4, v2
	v_cmp_ne_u32_e32 vcc, v3, v2
	s_and_saveexec_b64 s[6:7], vcc
	s_xor_b64 s[6:7], exec, s[6:7]
	s_cbranch_execz .LBB0_1069
	s_waitcnt lgkmcnt(0)
	v_mov_b32_e32 v0, 0x7000
	global_load_dword v0, v0, s[54:55] offset:1280 sc1
	s_add_u32 s12, s54, 0x7500
	s_addc_u32 s13, s55, 0
	s_waitcnt vmcnt(0)
	v_cmp_eq_u32_e32 vcc, v0, v1
	s_and_saveexec_b64 s[8:9], vcc
	s_cbranch_execz .LBB0_1068
	s_add_u32 s10, s54, 0x4200
	s_addc_u32 s11, s55, 0
	s_mov_b32 s24, 1
	s_mov_b64 s[14:15], 0
	v_mov_b32_e32 v0, 0
	s_branch .LBB0_1059

.LBB0_1125:
	s_or_b64 exec, exec, s[6:7]
	v_cvt_f32_u32_e32 v4, v2
	s_waitcnt vmcnt(0)
	v_readfirstlane_b32 s4, v3
	v_sub_u32_e32 v3, 0, v2
	v_rcp_iflag_f32_e32 v4, v4
	v_add_u32_e32 v5, s4, v1
	v_mul_f32_e32 v4, 0x4f7ffffe, v4
	v_cvt_u32_f32_e32 v4, v4
	v_mul_lo_u32 v1, v3, v4
	v_mul_hi_u32 v1, v4, v1
	v_add_u32_e32 v1, v4, v1
	v_mul_hi_u32 v1, v5, v1
	v_mul_lo_u32 v3, v1, v2
	v_sub_u32_e32 v3, v5, v3
	v_add_u32_e32 v4, 1, v1
	v_cmp_ge_u32_e32 vcc, v3, v2
	s_nop 1
	v_cndmask_b32_e32 v1, v1, v4, vcc
	v_sub_u32_e32 v4, v3, v2
	v_cndmask_b32_e32 v3, v3, v4, vcc
	v_add_u32_e32 v4, 1, v1
	v_cmp_ge_u32_e32 vcc, v3, v2
	v_add_u32_e32 v3, 1, v5
	s_nop 0
	v_cndmask_b32_e32 v1, v1, v4, vcc
	v_mul_lo_u32 v4, v2, v1
	v_add_u32_e32 v2, v4, v2
	v_cmp_ne_u32_e32 vcc, v3, v2
	s_and_saveexec_b64 s[4:5], vcc
	s_xor_b64 s[4:5], exec, s[4:5]
	s_cbranch_execz .LBB0_1139
	s_waitcnt lgkmcnt(0)
	v_mov_b32_e32 v0, 0x7000
	global_load_dword v0, v0, s[54:55] offset:1280 sc1
	s_add_u32 s10, s54, 0x7500
	s_addc_u32 s11, s55, 0
	s_waitcnt vmcnt(0)
	v_cmp_eq_u32_e32 vcc, v0, v1
	s_and_saveexec_b64 s[6:7], vcc
	s_cbranch_execz .LBB0_1138
	s_add_u32 s8, s54, 0x4200
	s_addc_u32 s9, s55, 0
	s_mov_b32 s22, 1
	s_mov_b64 s[12:13], 0
	v_mov_b32_e32 v0, 0
	s_branch .LBB0_1129

.LBB0_1156:
	s_or_b64 exec, exec, s[4:5]
	s_mov_b64 s[4:5], exec
	v_mbcnt_lo_u32_b32 v0, s4, 0
	v_mbcnt_hi_u32_b32 v0, s5, v0
	v_cmp_eq_u32_e32 vcc, 0, v0
	s_waitcnt vmcnt(0)
	buffer_inv sc1
	s_and_saveexec_b64 s[6:7], vcc
	s_cbranch_execz .LBB0_1158
	s_bcnt1_i32_b64 s4, s[4:5]
	v_mov_b32_e32 v0, 0x2000
	v_mov_b32_e32 v1, s4
	s_nop 0
	s_nop 0

.LBB0_1160:
	s_add_u32 s0, s54, 0x10000
	s_addc_u32 s1, s55, 0
	s_add_u32 s8, s54, 0x36200000
	s_addc_u32 s9, s55, 0
	s_add_u32 s10, s54, 0x3900000
	s_addc_u32 s11, s55, 0
	s_add_u32 s20, s54, 0x1100000
	s_addc_u32 s21, s55, 0
	s_add_u32 s22, s54, 0x16200000
	s_addc_u32 s23, s55, 0
	s_add_u32 s12, s54, 0x36200080
	s_addc_u32 s13, s55, 0
	s_ashr_i32 s73, s72, 31
	s_add_u32 s84, s54, 0x4200
	s_addc_u32 s85, s55, 0
	s_add_u32 s42, s54, 0x4400
	s_addc_u32 s43, s55, 0
	s_add_u32 s44, s54, 0x4500
	s_addc_u32 s45, s55, 0
	s_add_u32 s66, s54, 0x4600
	s_addc_u32 s67, s55, 0
	s_add_u32 s68, s54, 0x4700
	s_addc_u32 s69, s55, 0
	s_add_u32 s70, s54, 0x4800
	s_addc_u32 s71, s55, 0
	s_add_u32 s78, s54, 0x4900
	s_addc_u32 s79, s55, 0
	s_add_u32 s80, s54, 0x4a00
	s_addc_u32 s81, s55, 0
	s_add_u32 s86, s54, 0x4b00
	s_addc_u32 s87, s55, 0
	s_mov_b64 s[6:7], s[88:89]
	s_add_u32 s88, s54, 0x4c00
	s_addc_u32 s89, s55, 0
	s_add_u32 s90, s54, 0x4d00
	s_addc_u32 s91, s55, 0
	s_add_u32 s92, s54, 0x4e00
	s_addc_u32 s93, s55, 0
	s_add_u32 s94, s54, 0x4f00
	s_addc_u32 s95, s55, 0
	s_add_u32 s96, s54, 0x5000
	s_addc_u32 s97, s55, 0
	s_add_u32 s74, s54, 0x5100
	s_addc_u32 s75, s55, 0
	s_add_u32 s2, s54, 0x5200
	v_writelane_b32 v254, s0, 15
	s_addc_u32 s3, s55, 0
	s_add_u32 s4, s54, 0x5300
	v_writelane_b32 v254, s1, 16
	s_addc_u32 s5, s55, 0
	v_readlane_b32 s0, v254, 4
	s_cmp_eq_u32 s0, 15
	s_cselect_b64 s[14:15], -1, 0
	v_writelane_b32 v254, s14, 32
	s_cmp_eq_u32 s0, 14
	s_nop 0
	v_writelane_b32 v254, s15, 33
	s_cselect_b64 s[14:15], -1, 0
	v_writelane_b32 v254, s14, 34
	s_cmp_eq_u32 s0, 13
	s_nop 0
	v_writelane_b32 v254, s15, 35
	s_cselect_b64 s[14:15], -1, 0
	v_writelane_b32 v254, s14, 36
	s_cmp_eq_u32 s0, 12
	s_nop 0
	v_writelane_b32 v254, s15, 37
	s_cselect_b64 s[14:15], -1, 0
	v_writelane_b32 v254, s14, 38
	s_cmp_eq_u32 s0, 11
	s_nop 0
	v_writelane_b32 v254, s15, 39
	s_cselect_b64 s[14:15], -1, 0
	v_writelane_b32 v254, s14, 40
	s_cmp_eq_u32 s0, 10
	s_nop 0
	v_writelane_b32 v254, s15, 41
	s_cselect_b64 s[14:15], -1, 0
	v_writelane_b32 v254, s14, 42
	s_cmp_eq_u32 s0, 9
	s_nop 0
	v_writelane_b32 v254, s15, 43
	s_cselect_b64 s[14:15], -1, 0
	v_writelane_b32 v254, s14, 44
	s_cmp_eq_u32 s0, 8
	s_nop 0
	v_writelane_b32 v254, s15, 45
	s_cselect_b64 s[14:15], -1, 0
	v_writelane_b32 v254, s14, 46
	s_cmp_eq_u32 s0, 7
	s_nop 0
	v_writelane_b32 v254, s15, 47
	s_cselect_b64 s[14:15], -1, 0
	v_writelane_b32 v254, s14, 48
	s_cmp_eq_u32 s0, 6
	s_nop 0
	v_writelane_b32 v254, s15, 49
	s_cselect_b64 s[14:15], -1, 0
	v_writelane_b32 v254, s14, 50
	s_cmp_eq_u32 s0, 5
	s_nop 0
	v_writelane_b32 v254, s15, 51
	s_cselect_b64 s[14:15], -1, 0
	v_writelane_b32 v254, s14, 52
	s_cmp_eq_u32 s0, 4
	s_nop 0
	v_writelane_b32 v254, s15, 53
	s_cselect_b64 s[14:15], -1, 0
	v_writelane_b32 v254, s14, 54
	s_cmp_eq_u32 s0, 3
	s_nop 0
	v_writelane_b32 v254, s15, 55
	s_cselect_b64 s[14:15], -1, 0
	v_writelane_b32 v254, s14, 56
	s_cmp_eq_u32 s0, 2
	s_nop 0
	v_writelane_b32 v254, s15, 57
	s_cselect_b64 s[14:15], -1, 0
	v_writelane_b32 v254, s14, 58
	s_cmp_eq_u32 s0, 1
	s_nop 0
	v_writelane_b32 v254, s15, 59
	s_cselect_b64 s[14:15], -1, 0
	v_writelane_b32 v254, s14, 60
	s_cmp_eq_u32 s0, 0
	s_nop 0
	v_writelane_b32 v254, s15, 61
	s_cselect_b64 s[14:15], -1, 0
	s_lshl_b32 s0, s0, 8
	s_add_u32 s0, s6, s0
	s_addc_u32 s1, s7, 0
	s_add_u32 s6, s0, 0x1400
	s_addc_u32 s7, s1, 0
	s_add_u32 s38, s54, 0x7500
	s_addc_u32 s39, s55, 0
	s_add_u32 s0, s54, 0x7400
	s_addc_u32 s1, s55, 0
	s_add_u32 s40, s54, 0x7500
	v_writelane_b32 v255, s0, 0
	s_addc_u32 s41, s55, 0
	s_ashr_i32 s76, s33, 31
	v_writelane_b32 v254, s14, 62
	v_writelane_b32 v255, s1, 1
	s_lshr_b32 s0, s76, 29
	v_writelane_b32 v254, s15, 63
	s_add_i32 s0, s33, s0
	v_writelane_b32 v254, s6, 28
	s_ashr_i32 s37, s0, 3
	s_and_b32 s0, s0, -8
	v_writelane_b32 v254, s7, 29
	s_sub_i32 s0, s33, s0
	v_writelane_b32 v254, s0, 25
	s_nop 0
	v_readlane_b32 s24, v254, 11
	v_readlane_b32 s25, v254, 12
	v_writelane_b32 v254, s38, 4
	s_cmp_lt_i32 s24, 14
	s_cselect_b64 s[0:1], -1, 0
	v_writelane_b32 v254, s39, 5
	v_writelane_b32 v254, s40, 2
	s_cmp_gt_i32 s25, 13
	s_cselect_b64 s[6:7], -1, 0
	v_writelane_b32 v254, s41, 3
	v_writelane_b32 v254, s42, 17
	s_and_b64 s[0:1], s[0:1], s[6:7]
	s_andn2_b64 vcc, exec, s[0:1]
	v_writelane_b32 v254, s43, 18
	v_writelane_b32 v254, s44, 9
	s_nop 1
	v_writelane_b32 v254, s45, 10
	v_writelane_b32 v254, s66, 13
	s_nop 1
	v_writelane_b32 v254, s67, 14
	v_writelane_b32 v254, s68, 19
	s_nop 1
	v_writelane_b32 v254, s69, 20
	v_writelane_b32 v254, s70, 30
	s_nop 1
	v_writelane_b32 v254, s71, 31
	v_writelane_b32 v254, s78, 21
	s_nop 1
	v_writelane_b32 v254, s79, 22
	v_writelane_b32 v254, s80, 23
	s_nop 1
	v_writelane_b32 v254, s81, 24
	s_cbranch_vccnz .LBB0_1245
	v_mbcnt_hi_u32_b32 v0, -1, v248
	s_waitcnt lgkmcnt(0)
	v_lshlrev_b32_e32 v1, 8, v0
	v_readlane_b32 s0, v254, 15
	v_and_b32_e32 v1, 0xf00, v1
	v_readlane_b32 s1, v254, 16
	s_nop 4
	global_load_dword v1, v1, s[0:1] sc1
	v_readlane_b32 s0, v254, 8
	s_waitcnt vmcnt(0)
	v_readlane_b32 s1, v1, 1
	v_add_u32_e32 v7, s0, v0
	v_readlane_b32 s0, v1, 0
	v_readlane_b32 s6, v1, 2
	s_addk_i32 s0, 0xff
	s_addk_i32 s1, 0xff
	v_readlane_b32 s7, v1, 3
	s_addk_i32 s6, 0xff
	s_lshr_b32 s46, s0, 8
	s_lshr_b32 s47, s1, 8
	v_readlane_b32 s14, v1, 4
	s_addk_i32 s7, 0xff
	s_lshr_b32 s48, s6, 8
	s_add_i32 s47, s47, s46
	v_readlane_b32 s15, v1, 5
	s_addk_i32 s14, 0xff
	s_lshr_b32 s49, s7, 8
	s_add_i32 s48, s48, s47
	v_readlane_b32 s16, v1, 6
	s_addk_i32 s15, 0xff
	s_lshr_b32 s50, s14, 8
	s_add_i32 s49, s49, s48
	v_readlane_b32 s17, v1, 7
	s_addk_i32 s16, 0xff
	s_lshr_b32 s51, s15, 8
	s_add_i32 s50, s50, s49
	s_addk_i32 s17, 0xff
	s_lshr_b32 s62, s16, 8
	s_add_i32 s51, s51, s50
	s_lshr_b32 s63, s17, 8
	s_add_i32 s62, s62, s51
	s_add_i32 s63, s63, s62
	s_mul_i32 s26, s63, 28
	s_cmp_ge_i32 s33, s26
	v_readfirstlane_b32 s30, v7
	s_cbranch_scc1 .LBB0_1191
	s_lshr_b32 s77, s26, 3
	v_writelane_b32 v255, s86, 2
	s_and_b32 s64, s26, 4
	s_add_i32 s65, s77, 1
	v_readlane_b32 s0, v254, 25
	v_writelane_b32 v255, s87, 3
	s_cmp_ge_i32 s0, s64
	s_mul_i32 s1, s65, s64
	s_cbranch_scc0 .LBB0_1164
	s_sub_i32 s0, s0, s64
	s_mul_i32 s0, s0, s77
	s_mov_b32 s86, s1
	s_add_i32 s6, s0, s1
	s_cbranch_execz .LBB0_1165
	s_branch .LBB0_1166

.LBB0_1241:
	s_or_b64 exec, exec, s[14:15]
	s_mov_b64 s[14:15], exec
	v_mbcnt_lo_u32_b32 v0, s14, 0
	v_mbcnt_hi_u32_b32 v0, s15, v0
	v_cmp_eq_u32_e32 vcc, 0, v0
	s_waitcnt vmcnt(0)
	buffer_inv sc1
	s_and_saveexec_b64 s[16:17], vcc
	s_cbranch_execz .LBB0_1243
	s_bcnt1_i32_b64 s6, s[14:15]
	v_mov_b32_e32 v0, 0
	v_mov_b32_e32 v1, s6
	s_nop 0
	s_nop 0

.LBB0_1351:
	s_or_b64 exec, exec, s[8:9]
	s_mov_b64 s[8:9], exec
	v_mbcnt_lo_u32_b32 v0, s8, 0
	v_mbcnt_hi_u32_b32 v0, s9, v0
	v_cmp_eq_u32_e32 vcc, 0, v0
	s_waitcnt vmcnt(0)
	buffer_inv sc1
	s_and_saveexec_b64 s[10:11], vcc
	s_cbranch_execz .LBB0_1353
	s_bcnt1_i32_b64 s6, s[8:9]
	v_mov_b32_e32 v0, 0
	v_mov_b32_e32 v1, s6
	s_nop 0
	s_nop 0

.LBB0_1430:
	s_or_b64 exec, exec, s[2:3]
	s_mov_b64 s[2:3], exec
	v_mbcnt_lo_u32_b32 v0, s2, 0
	v_mbcnt_hi_u32_b32 v0, s3, v0
	v_cmp_eq_u32_e32 vcc, 0, v0
	s_waitcnt vmcnt(0)
	buffer_inv sc1
	s_and_saveexec_b64 s[4:5], vcc
	s_cbranch_execz .LBB0_1432
	s_bcnt1_i32_b64 s2, s[2:3]
	v_mov_b32_e32 v0, 0
	v_mov_b32_e32 v1, s2
	s_nop 0
	s_nop 0
